# y-phase epilogue: 6 v_pk_mul_f32 split into scalar v_mul_f32 pairs
# baseline (speedup 1.0000x reference)
.LBB1_4:
	s_or_b64 exec, exec, s[4:5]
	v_lshl_or_b32 v4, v27, 1, v96
	v_lshl_or_b32 v3, v4, 7, v3
	v_or_b32_e32 v5, 0x23600, v3
	v_or_b32_e32 v3, 0x23640, v3
	s_waitcnt lgkmcnt(0)
	s_barrier
	ds_read_b32 v5, v5
	ds_read_b32 v3, v3
	v_lshrrev_b32_e32 v216, 5, v126
	v_and_b32_e32 v217, 3, v216
	v_lshrrev_b32_e32 v216, 2, v216
	v_and_b32_e32 v216, 1, v216
	v_mul_u32_u24_e32 v216, 0x60, v216
	v_lshl_add_u32 v216, v119, 3, v216
	v_bfe_u32 v218, v116, 2, 2
	v_add_u32_e32 v216, v216, v218
	v_lshlrev_b32_e32 v216, 8, v216
	v_lshrrev_b32_e32 v219, 1, v217
	v_mul_u32_u24_e32 v219, 0xc000, v219
	v_add_u32_e32 v216, v216, v219
	v_and_b32_e32 v217, 1, v217
	v_lshlrev_b32_e32 v217, 3, v217
	v_bfe_u32 v219, v116, 4, 1
	v_lshl_or_b32 v217, v219, 1, v217
	v_bfe_u32 v219, v116, 1, 1
	v_or_b32_e32 v217, v217, v219
	v_lshlrev_b32_e32 v218, 2, v218
	v_lshl_or_b32 v218, v119, 1, v218
	v_xor_b32_e32 v217, v217, v218
	v_lshl_or_b32 v216, v217, 4, v216
	v_and_b32_e32 v217, 1, v116
	v_lshl_or_b32 v212, v217, 3, v216
	v_xor_b32_e32 v213, 16, v212
	v_add_u32_e32 v213, 0x400, v213
	v_xor_b32_e32 v214, 64, v212
	v_xor_b32_e32 v215, 64, v213
	v_mad_u32_u24 v4, v4, s7, v13
	v_lshl_add_u32 v4, v119, 4, v4
	v_or_b32_e32 v6, 0x20000, v4
	ds_read_b128 v[16:19], v6
	s_waitcnt lgkmcnt(1)
	v_add_f32_e32 v3, v5, v3
	v_add_u32_e32 v5, 0x20020, v4
	v_add_u32_e32 v6, 0x20040, v4
	ds_read_b128 v[112:115], v5
	ds_read_b128 v[108:111], v6
	v_add_u32_e32 v5, 0x20060, v4
	v_add_u32_e32 v6, 0x20080, v4
	ds_read_b128 v[104:107], v5
	ds_read_b128 v[96:99], v6
	v_and_b32_e32 v164, 8, v121
	v_add_u32_e32 v4, 0x200a0, v4
	ds_read_b128 v[100:103], v4
	ds_read_b64_tr_b16 v[4:5], v212
	ds_read_b64_tr_b16 v[6:7], v213
	ds_read_b64_tr_b16 v[20:21], v212 offset:4096
	ds_read_b64_tr_b16 v[22:23], v213 offset:4096
	ds_read_b64_tr_b16 v[28:29], v212 offset:8192
	ds_read_b64_tr_b16 v[30:31], v213 offset:8192
	ds_read_b64_tr_b16 v[128:129], v212 offset:12288
	ds_read_b64_tr_b16 v[130:131], v213 offset:12288
	ds_read_b64_tr_b16 v[132:133], v212 offset:16384
	ds_read_b64_tr_b16 v[134:135], v213 offset:16384
	ds_read_b64_tr_b16 v[136:137], v212 offset:20480
	ds_read_b64_tr_b16 v[138:139], v213 offset:20480
	ds_read_b64_tr_b16 v[140:141], v214
	ds_read_b64_tr_b16 v[142:143], v215
	ds_read_b64_tr_b16 v[144:145], v214 offset:4096
	ds_read_b64_tr_b16 v[146:147], v215 offset:4096
	ds_read_b64_tr_b16 v[148:149], v214 offset:8192
	ds_read_b64_tr_b16 v[150:151], v215 offset:8192
	ds_read_b64_tr_b16 v[152:153], v214 offset:12288
	ds_read_b64_tr_b16 v[154:155], v215 offset:12288
	ds_read_b64_tr_b16 v[156:157], v214 offset:16384
	v_div_scale_f32 v1, s[8:9], v3, v3, 1.0
	v_rcp_f32_e32 v9, v1
	ds_read_b64_tr_b16 v[158:159], v215 offset:16384
	ds_read_b64_tr_b16 v[160:161], v214 offset:20480
	ds_read_b64_tr_b16 v[162:163], v215 offset:20480
	s_mov_b32 s4, 0xc000
	s_movk_i32 s5, 0x4000
	v_fma_f32 v0, -v1, v9, 1.0
	v_fmac_f32_e32 v9, v0, v9
	v_div_scale_f32 v0, vcc, 1.0, v3, 1.0
	v_mul_f32_e32 v2, v0, v9
	v_fma_f32 v8, -v1, v2, v0
	v_fmac_f32_e32 v2, v8, v9
	v_fma_f32 v0, -v1, v2, v0
	v_div_fmas_f32 v0, v0, v9, v2
	v_div_fixup_f32 v124, v0, v3, 1.0
	s_waitcnt lgkmcnt(14)
	v_mfma_f32_32x32x16_f16 v[0:15], v[4:7], v[16:19], 0
	s_mov_b32 s7, 0x18000
	v_lshlrev_b32_e32 v172, 2, v126
	v_mov_b32_e32 v173, 0
	v_mfma_f32_32x32x16_f16 v[0:15], v[20:23], v[112:115], v[0:15]
	v_or_b32_e32 v20, v26, v116
	v_and_b32_e32 v21, 0x4000, v118
	v_lshl_or_b32 v20, v20, 8, v21
	v_bitop3_b32 v118, v121, v120, 8 bitop3:0x6c
	v_or3_b32 v121, v20, v125, s7
	v_mfma_f32_32x32x16_f16 v[0:15], v[28:31], v[108:111], v[0:15]
	v_mfma_f32_32x32x16_f16 v[0:15], v[128:131], v[104:107], v[0:15]
	v_mfma_f32_32x32x16_f16 v[0:15], v[132:135], v[96:99], v[0:15]
	s_waitcnt lgkmcnt(12)
	v_mfma_f32_32x32x16_f16 v[0:15], v[136:139], v[100:103], v[0:15]
	s_nop 11
	v_fma_mixlo_f16 v20, v124, v0, 0
	v_mov_b32_e32 v0, v1
	v_mov_b32_e32 v1, v2
	v_mul_f32_e32 v0, v124, v0
	v_mul_f32_e32 v1, v124, v1
	v_cvt_pk_f16_f32 v1, v0, v1
	v_pack_b32_f16 v0, v20, v1
	s_waitcnt lgkmcnt(10)
	v_mfma_f32_32x32x16_f16 v[16:31], v[140:143], v[16:19], 0
	v_fma_mixlo_f16 v2, v124, v3, 0
	v_alignbit_b32 v1, v2, v1, 16
	v_lshl_or_b32 v2, v118, 4, v121
	ds_write_b64 v2, v[0:1]
	v_mov_b32_e32 v0, v5
	v_mov_b32_e32 v1, v6
	v_mul_f32_e32 v0, v124, v0
	v_mul_f32_e32 v1, v124, v1
	s_waitcnt lgkmcnt(9)
	v_mfma_f32_32x32x16_f16 v[16:31], v[144:147], v[112:115], v[16:31]
	v_fma_mixlo_f16 v2, v124, v4, 0
	v_cvt_pk_f16_f32 v1, v0, v1
	v_pack_b32_f16 v0, v2, v1
	v_fma_mixlo_f16 v2, v124, v7, 0
	v_alignbit_b32 v1, v2, v1, 16
	v_bitop3_b32 v2, v164, v120, 1 bitop3:0x36
	v_lshl_or_b32 v2, v2, 4, v121
	s_waitcnt lgkmcnt(7)
	v_mfma_f32_32x32x16_f16 v[16:31], v[148:151], v[108:111], v[16:31]
	ds_write_b64 v2, v[0:1]
	v_mov_b32_e32 v0, v9
	v_mov_b32_e32 v1, v10
	v_mul_f32_e64 v0, v124, v0
	v_mul_f32_e64 v1, v124, v1
	v_fma_mixlo_f16 v2, v124, v8, 0
	v_cvt_pk_f16_f32 v1, v0, v1
	v_pack_b32_f16 v0, v2, v1
	s_waitcnt lgkmcnt(6)
	v_mfma_f32_32x32x16_f16 v[16:31], v[152:155], v[104:107], v[16:31]
	v_fma_mixlo_f16 v2, v124, v11, 0
	v_alignbit_b32 v1, v2, v1, 16
	v_bitop3_b32 v2, v164, v120, 2 bitop3:0x36
	v_lshl_or_b32 v2, v2, 4, v121
	ds_write_b64 v2, v[0:1]
	v_mov_b32_e32 v0, v13
	v_mov_b32_e32 v1, v14
	s_waitcnt lgkmcnt(5)
	v_mfma_f32_32x32x16_f16 v[16:31], v[156:159], v[96:99], v[16:31]
	v_mul_f32_e64 v0, v124, v0
	v_mul_f32_e64 v1, v124, v1
	v_fma_mixlo_f16 v2, v124, v12, 0
	v_cvt_pk_f16_f32 v1, v0, v1
	v_pack_b32_f16 v0, v2, v1
	v_fma_mixlo_f16 v2, v124, v15, 0
	v_alignbit_b32 v1, v2, v1, 16
	v_bitop3_b32 v2, v164, v120, 3 bitop3:0x36
	s_waitcnt lgkmcnt(3)
	v_mfma_f32_32x32x16_f16 v[16:31], v[160:163], v[100:103], v[16:31]
	v_lshl_or_b32 v2, v2, 4, v121
	ds_write_b64 v2, v[0:1]
	s_nop 9
	v_mov_b32_e32 v0, v17
	v_mov_b32_e32 v1, v18
	v_mul_f32_e32 v0, v124, v0
	v_mul_f32_e32 v1, v124, v1
	v_fma_mixlo_f16 v2, v124, v16, 0
	v_cvt_pk_f16_f32 v1, v0, v1
	v_pack_b32_f16 v0, v2, v1
	v_fma_mixlo_f16 v2, v124, v19, 0
	v_alignbit_b32 v1, v2, v1, 16
	v_bitop3_b32 v2, v164, v120, 4 bitop3:0x36
	v_lshl_or_b32 v2, v2, 4, v121
	ds_write_b64 v2, v[0:1]
	v_mov_b32_e32 v0, v21
	v_mov_b32_e32 v1, v22
	v_mul_f32_e32 v0, v124, v0
	v_mul_f32_e32 v1, v124, v1
	v_fma_mixlo_f16 v2, v124, v20, 0
	v_cvt_pk_f16_f32 v1, v0, v1
	v_pack_b32_f16 v0, v2, v1
	v_fma_mixlo_f16 v2, v124, v23, 0
	v_alignbit_b32 v1, v2, v1, 16
	v_bitop3_b32 v2, v164, v120, 5 bitop3:0x36
	v_lshl_or_b32 v2, v2, 4, v121
	ds_write_b64 v2, v[0:1]
	v_mov_b32_e32 v0, v25
	v_mov_b32_e32 v1, v26
	v_mul_f32_e32 v0, v124, v0
	v_mul_f32_e32 v1, v124, v1
	v_fma_mixlo_f16 v2, v124, v24, 0
	v_cvt_pk_f16_f32 v1, v0, v1
	v_pack_b32_f16 v0, v2, v1
	v_fma_mixlo_f16 v2, v124, v27, 0
	v_alignbit_b32 v1, v2, v1, 16
	v_bitop3_b32 v2, v164, v120, 6 bitop3:0x36
	v_lshl_or_b32 v2, v2, 4, v121
	ds_write_b64 v2, v[0:1]
	v_mov_b32_e32 v0, v29
	v_mov_b32_e32 v1, v30
	v_mul_f32_e32 v0, v124, v0
	v_mul_f32_e32 v1, v124, v1
	v_fma_mixlo_f16 v2, v124, v28, 0
	v_cvt_pk_f16_f32 v1, v0, v1
	v_pack_b32_f16 v0, v2, v1
	v_fma_mixlo_f16 v2, v124, v31, 0
	v_alignbit_b32 v1, v2, v1, 16
	v_bitop3_b32 v2, v164, v120, 7 bitop3:0x36
	v_lshl_or_b32 v2, v2, 4, v121
	ds_write_b64 v2, v[0:1]
	v_lshl_add_u64 v[0:1], s[0:1], 0, v[172:173]
	v_lshlrev_b32_e32 v172, 2, v127
	v_lshl_add_u64 v[0:1], v[0:1], 0, v[172:173]
	s_waitcnt lgkmcnt(0)
	s_barrier
	v_and_b32_e32 v245, 15, v116
	v_lshrrev_b32_e32 v246, 4, v116
	v_lshl_or_b32 v246, v119, 1, v246
	v_lshrrev_b32_e32 v250, 5, v126
	v_and_b32_e32 v250, 7, v250
	v_and_b32_e32 v247, 1, v246
	v_lshrrev_b32_e32 v248, 1, v246
	v_xor_b32_e32 v248, v248, v247
	v_lshl_or_b32 v247, v247, 1, v248
	v_and_b32_e32 v248, 3, v245
	v_lshrrev_b32_e32 v249, 2, v245
	v_lshl_or_b32 v248, v248, 2, v249
	v_xor_b32_e32 v247, v247, v248
	v_lshlrev_b32_e32 v240, 8, v245
	v_lshl_or_b32 v240, v247, 4, v240
	v_add_u32_e32 v240, 0x18000, v240
	v_xor_b32_e32 v241, 64, v240
	v_xor_b32_e32 v242, 0x80, v240
	v_xor_b32_e32 v243, 0xc0, v240
	v_lshlrev_b32_e32 v249, 7, v250
	v_lshl_or_b32 v249, v246, 4, v249
	v_and_b32_e32 v249, 0x3f0, v249
	global_load_dwordx4 v[96:99], v249, s[34:35]
	global_load_dwordx4 v[100:103], v249, s[34:35] offset:64
	v_lshlrev_b32_e32 v244, 19, v250
	v_lshl_or_b32 v244, v246, 16, v244
	v_lshl_or_b32 v244, v245, 3, v244
	v_and_b32_e32 v244, 0x3fff78, v244
	s_lshl_b64 s[22:23], s[2:3], 22
	s_add_u32 s22, s22, s30
	s_addc_u32 s23, s23, s31
	s_lshl_b32 s24, s14, 3
	s_add_u32 s22, s22, s24
	s_addc_u32 s23, s23, 0
	ds_read_b128 v[112:115], v240
	ds_read_b128 v[144:147], v240 offset:8192
	ds_read_b128 v[116:119], v241
	ds_read_b128 v[148:151], v241 offset:8192
	ds_read_b128 v[120:123], v242
	ds_read_b128 v[152:155], v242 offset:8192
	ds_read_b128 v[124:127], v243
	ds_read_b128 v[156:159], v243 offset:8192
	ds_read_b128 v[128:131], v240 offset:16384
	ds_read_b128 v[160:163], v240 offset:24576
	ds_read_b128 v[132:135], v241 offset:16384
	ds_read_b128 v[164:167], v241 offset:24576
	ds_read_b128 v[136:139], v242 offset:16384
	ds_read_b128 v[168:171], v242 offset:24576
	ds_read_b128 v[140:143], v243 offset:16384
	ds_read_b128 v[172:175], v243 offset:24576
	s_waitcnt vmcnt(2)
	s_waitcnt lgkmcnt(14)
	v_mfma_f32_16x16x32_f16 v[0:3], v[36:39], v[112:115], 0
	v_mfma_f32_16x16x32_f16 v[4:7], v[36:39], v[144:147], 0
	v_mfma_f32_16x16x32_f16 v[8:11], v[76:79], v[112:115], 0
	v_mfma_f32_16x16x32_f16 v[12:15], v[76:79], v[144:147], 0
	s_waitcnt lgkmcnt(12)
	v_mfma_f32_16x16x32_f16 v[0:3], v[32:35], v[116:119], v[0:3]
	v_mfma_f32_16x16x32_f16 v[4:7], v[32:35], v[148:151], v[4:7]
	v_mfma_f32_16x16x32_f16 v[8:11], v[72:75], v[116:119], v[8:11]
	v_mfma_f32_16x16x32_f16 v[12:15], v[72:75], v[148:151], v[12:15]
	s_waitcnt lgkmcnt(10)
	v_mfma_f32_16x16x32_f16 v[0:3], v[64:67], v[120:123], v[0:3]
	v_mfma_f32_16x16x32_f16 v[4:7], v[64:67], v[152:155], v[4:7]
	v_mfma_f32_16x16x32_f16 v[8:11], v[68:71], v[120:123], v[8:11]
	v_mfma_f32_16x16x32_f16 v[12:15], v[68:71], v[152:155], v[12:15]
	s_waitcnt lgkmcnt(8)
	v_mfma_f32_16x16x32_f16 v[0:3], v[48:51], v[124:127], v[0:3]
	v_mfma_f32_16x16x32_f16 v[4:7], v[48:51], v[156:159], v[4:7]
	v_mfma_f32_16x16x32_f16 v[8:11], v[52:55], v[124:127], v[8:11]
	v_mfma_f32_16x16x32_f16 v[12:15], v[52:55], v[156:159], v[12:15]
	s_waitcnt lgkmcnt(6)
	v_mfma_f32_16x16x32_f16 v[0:3], v[92:95], v[128:131], v[0:3]
	v_mfma_f32_16x16x32_f16 v[4:7], v[92:95], v[160:163], v[4:7]
	v_mfma_f32_16x16x32_f16 v[8:11], v[60:63], v[128:131], v[8:11]
	v_mfma_f32_16x16x32_f16 v[12:15], v[60:63], v[160:163], v[12:15]
	s_waitcnt lgkmcnt(4)
	v_mfma_f32_16x16x32_f16 v[0:3], v[84:87], v[132:135], v[0:3]
	v_mfma_f32_16x16x32_f16 v[4:7], v[84:87], v[164:167], v[4:7]
	v_mfma_f32_16x16x32_f16 v[8:11], v[56:59], v[132:135], v[8:11]
	v_mfma_f32_16x16x32_f16 v[12:15], v[56:59], v[164:167], v[12:15]
	s_waitcnt lgkmcnt(2)
	v_mfma_f32_16x16x32_f16 v[0:3], v[80:83], v[136:139], v[0:3]
	v_mfma_f32_16x16x32_f16 v[4:7], v[80:83], v[168:171], v[4:7]
	v_mfma_f32_16x16x32_f16 v[8:11], v[44:47], v[136:139], v[8:11]
	v_mfma_f32_16x16x32_f16 v[12:15], v[44:47], v[168:171], v[12:15]
	s_waitcnt lgkmcnt(0)
	v_mfma_f32_16x16x32_f16 v[0:3], v[88:91], v[140:143], v[0:3]
	v_mfma_f32_16x16x32_f16 v[4:7], v[88:91], v[172:175], v[4:7]
	v_mfma_f32_16x16x32_f16 v[8:11], v[40:43], v[140:143], v[8:11]
	v_mfma_f32_16x16x32_f16 v[12:15], v[40:43], v[172:175], v[12:15]
	ds_read_b128 v[176:179], v240 offset:4096
	ds_read_b128 v[208:211], v240 offset:12288
	ds_read_b128 v[180:183], v241 offset:4096
	ds_read_b128 v[212:215], v241 offset:12288
	ds_read_b128 v[184:187], v242 offset:4096
	ds_read_b128 v[216:219], v242 offset:12288
	ds_read_b128 v[188:191], v243 offset:4096
	ds_read_b128 v[220:223], v243 offset:12288
	ds_read_b128 v[192:195], v240 offset:20480
	ds_read_b128 v[224:227], v240 offset:28672
	ds_read_b128 v[196:199], v241 offset:20480
	ds_read_b128 v[228:231], v241 offset:28672
	ds_read_b128 v[200:203], v242 offset:20480
	ds_read_b128 v[232:235], v242 offset:28672
	ds_read_b128 v[204:207], v243 offset:20480
	ds_read_b128 v[236:239], v243 offset:28672
	s_waitcnt vmcnt(0)
	s_waitcnt lgkmcnt(14)
	v_mfma_f32_16x16x32_f16 v[16:19], v[36:39], v[176:179], 0
	v_mfma_f32_16x16x32_f16 v[20:23], v[36:39], v[208:211], 0
	v_mfma_f32_16x16x32_f16 v[24:27], v[76:79], v[176:179], 0
	v_mfma_f32_16x16x32_f16 v[28:31], v[76:79], v[208:211], 0
	s_add_u32 s26, s22, 0x0
	s_addc_u32 s27, s23, 0
	v_add_f32_e32 v104, v0, v96
	v_add_f32_e32 v105, v4, v96
	global_store_dwordx2 v244, v[104:105], s[26:27] nt
	s_waitcnt lgkmcnt(12)
	v_mfma_f32_16x16x32_f16 v[16:19], v[32:35], v[180:183], v[16:19]
	v_mfma_f32_16x16x32_f16 v[20:23], v[32:35], v[212:215], v[20:23]
	v_mfma_f32_16x16x32_f16 v[24:27], v[72:75], v[180:183], v[24:27]
	v_mfma_f32_16x16x32_f16 v[28:31], v[72:75], v[212:215], v[28:31]
	s_add_u32 s26, s22, 0x4000
	s_addc_u32 s27, s23, 0
	v_add_f32_e32 v106, v1, v97
	v_add_f32_e32 v107, v5, v97
	global_store_dwordx2 v244, v[106:107], s[26:27] nt
	s_waitcnt lgkmcnt(10)
	v_mfma_f32_16x16x32_f16 v[16:19], v[64:67], v[184:187], v[16:19]
	v_mfma_f32_16x16x32_f16 v[20:23], v[64:67], v[216:219], v[20:23]
	v_mfma_f32_16x16x32_f16 v[24:27], v[68:71], v[184:187], v[24:27]
	v_mfma_f32_16x16x32_f16 v[28:31], v[68:71], v[216:219], v[28:31]
	s_add_u32 s26, s22, 0x8000
	s_addc_u32 s27, s23, 0
	v_add_f32_e32 v108, v2, v98
	v_add_f32_e32 v109, v6, v98
	global_store_dwordx2 v244, v[108:109], s[26:27] nt
	s_waitcnt lgkmcnt(8)
	v_mfma_f32_16x16x32_f16 v[16:19], v[48:51], v[188:191], v[16:19]
	v_mfma_f32_16x16x32_f16 v[20:23], v[48:51], v[220:223], v[20:23]
	v_mfma_f32_16x16x32_f16 v[24:27], v[52:55], v[188:191], v[24:27]
	v_mfma_f32_16x16x32_f16 v[28:31], v[52:55], v[220:223], v[28:31]
	s_add_u32 s26, s22, 0xc000
	s_addc_u32 s27, s23, 0
	v_add_f32_e32 v110, v3, v99
	v_add_f32_e32 v111, v7, v99
	global_store_dwordx2 v244, v[110:111], s[26:27] nt
	s_waitcnt lgkmcnt(6)
	v_mfma_f32_16x16x32_f16 v[16:19], v[92:95], v[192:195], v[16:19]
	v_mfma_f32_16x16x32_f16 v[20:23], v[92:95], v[224:227], v[20:23]
	v_mfma_f32_16x16x32_f16 v[24:27], v[60:63], v[192:195], v[24:27]
	v_mfma_f32_16x16x32_f16 v[28:31], v[60:63], v[224:227], v[28:31]
	s_add_u32 s26, s22, 0x40000
	s_addc_u32 s27, s23, 0
	v_add_f32_e32 v104, v8, v100
	v_add_f32_e32 v105, v12, v100
	global_store_dwordx2 v244, v[104:105], s[26:27] nt
	s_waitcnt lgkmcnt(4)
	v_mfma_f32_16x16x32_f16 v[16:19], v[84:87], v[196:199], v[16:19]
	v_mfma_f32_16x16x32_f16 v[20:23], v[84:87], v[228:231], v[20:23]
	v_mfma_f32_16x16x32_f16 v[24:27], v[56:59], v[196:199], v[24:27]
	v_mfma_f32_16x16x32_f16 v[28:31], v[56:59], v[228:231], v[28:31]
	s_add_u32 s26, s22, 0x44000
	s_addc_u32 s27, s23, 0
	v_add_f32_e32 v106, v9, v101
	v_add_f32_e32 v107, v13, v101
	global_store_dwordx2 v244, v[106:107], s[26:27] nt
	s_waitcnt lgkmcnt(2)
	v_mfma_f32_16x16x32_f16 v[16:19], v[80:83], v[200:203], v[16:19]
	v_mfma_f32_16x16x32_f16 v[20:23], v[80:83], v[232:235], v[20:23]
	v_mfma_f32_16x16x32_f16 v[24:27], v[44:47], v[200:203], v[24:27]
	v_mfma_f32_16x16x32_f16 v[28:31], v[44:47], v[232:235], v[28:31]
	s_add_u32 s26, s22, 0x48000
	s_addc_u32 s27, s23, 0
	v_add_f32_e32 v108, v10, v102
	v_add_f32_e32 v109, v14, v102
	global_store_dwordx2 v244, v[108:109], s[26:27] nt
	s_waitcnt lgkmcnt(0)
	v_mfma_f32_16x16x32_f16 v[16:19], v[88:91], v[204:207], v[16:19]
	v_mfma_f32_16x16x32_f16 v[20:23], v[88:91], v[236:239], v[20:23]
	v_mfma_f32_16x16x32_f16 v[24:27], v[40:43], v[204:207], v[24:27]
	v_mfma_f32_16x16x32_f16 v[28:31], v[40:43], v[236:239], v[28:31]
	s_add_u32 s26, s22, 0x4c000
	s_addc_u32 s27, s23, 0
	v_add_f32_e32 v110, v11, v103
	v_add_f32_e32 v111, v15, v103
	global_store_dwordx2 v244, v[110:111], s[26:27] nt
	s_nop 7
	s_nop 1
	s_add_u32 s26, s22, 0x0
	s_addc_u32 s27, s23, 0
	v_add_f32_e32 v104, v16, v96
	v_add_f32_e32 v105, v20, v96
	global_store_dwordx2 v244, v[104:105], s[26:27] offset:128 nt
	s_add_u32 s26, s22, 0x4000
	s_addc_u32 s27, s23, 0
	v_add_f32_e32 v106, v17, v97
	v_add_f32_e32 v107, v21, v97
	global_store_dwordx2 v244, v[106:107], s[26:27] offset:128 nt
	s_add_u32 s26, s22, 0x8000
	s_addc_u32 s27, s23, 0
	v_add_f32_e32 v108, v18, v98
	v_add_f32_e32 v109, v22, v98
	global_store_dwordx2 v244, v[108:109], s[26:27] offset:128 nt
	s_add_u32 s26, s22, 0xc000
	s_addc_u32 s27, s23, 0
	v_add_f32_e32 v110, v19, v99
	v_add_f32_e32 v111, v23, v99
	global_store_dwordx2 v244, v[110:111], s[26:27] offset:128 nt
	s_add_u32 s26, s22, 0x40000
	s_addc_u32 s27, s23, 0
	v_add_f32_e32 v104, v24, v100
	v_add_f32_e32 v105, v28, v100
	global_store_dwordx2 v244, v[104:105], s[26:27] offset:128 nt
	s_add_u32 s26, s22, 0x44000
	s_addc_u32 s27, s23, 0
	v_add_f32_e32 v106, v25, v101
	v_add_f32_e32 v107, v29, v101
	global_store_dwordx2 v244, v[106:107], s[26:27] offset:128 nt
	s_add_u32 s26, s22, 0x48000
	s_addc_u32 s27, s23, 0
	v_add_f32_e32 v108, v26, v102
	v_add_f32_e32 v109, v30, v102
	global_store_dwordx2 v244, v[108:109], s[26:27] offset:128 nt
	s_add_u32 s26, s22, 0x4c000
	s_addc_u32 s27, s23, 0
	v_add_f32_e32 v110, v27, v103
	v_add_f32_e32 v111, v31, v103
	global_store_dwordx2 v244, v[110:111], s[26:27] offset:128 nt
	s_endpgm
